# attention unit epilogue: 32 serial ds_read_b32 of the softmax scale pairs replaced by 8 ds_read_b128; rms-norm lane reductions by DPP adds instead of ds_bpermute
# speedup vs baseline: 1.0182x; 1.0052x over previous
; #define LAS __attribute__((address_space(3)))
; template <class Mid> __device__ __forceinline__ void attn_unit(const Mid& mid, LAS unsigned char* lds, const bf16* __restrict__ Qu, const bf16* __restrict__ Kh, const bf16* __restrict__ Vh, int q0, int NT, ...
;     ...
;     LAS float* wsf = (LAS float*)(lds + FA_WS) + wid * 64;
;     if (hie == 0) { wsf[r32e] = 1.0f / l1; wsf[32 + r32e] = lam / l2; }
;     const LAS float* wq = wsf + 4 * hie;
;     LAS float* sb = (LAS float*)(lds + FA_OST) + wid * (32 * OST_PITCH) + (4 * hie) * OST_PITCH + r32e;
; #pragma unroll
;     for (int i = 0; i < 16; ++i) {
;         const int qc = (i & 3) + 8 * (i >> 2); const float a = wq[qc], b = wq[32 + qc];
;         sb[qc * OST_PITCH] = o1[0][i] * a - o2[0][i] * b; sb[qc * OST_PITCH + 32] = o1[1][i] * a - o2[1][i] * b;
;     }
;     const int ch = lane_e & 7;
;     const f32x4 g0 = *(const f32x4*)(subg + ch * 8), g1 = *(const f32x4*)(subg + ch * 8 + 4);
;     const LAS float* rb = (const LAS float*)(lds + FA_OST) + wid * (32 * OST_PITCH) + (lane_e >> 3) * OST_PITCH + ch * 8;
;     bf16* mrow = mixp + (size_t)(wid * 32 + (lane_e >> 3)) * DM + ch * 8;
; #pragma unroll
;     for (int ps = 0; ps < 4; ++ps) {
;         const f32x4 x0 = *(const LAS f32x4*)(rb + ps * 8 * OST_PITCH), x1 = *(const LAS f32x4*)(rb + ps * 8 * OST_PITCH + 4);
;         float ss = (x0[0] * x0[0] + x0[1] * x0[1]) + (x0[2] * x0[2] + x0[3] * x0[3]) + (x1[0] * x1[0] + x1[1] * x1[1]) + (x1[2] * x1[2] + x1[3] * x1[3]);
;         ss += __shfl_xor(ss, 1); ss += __shfl_xor(ss, 2); ss += __shfl_xor(ss, 4);
.LBB0_467:
	s_or_b64 exec, exec, s[30:31]
	v_ashrrev_i32_e32 v200, 3, v213
	v_and_b32_e32 v201, -4, v200
	s_waitcnt lgkmcnt(0)
	v_lshl_add_u32 v202, v201, 2, s34
	ds_read_b128 v[222:225], v202
	ds_read_b128 v[226:229], v202 offset:32
	ds_read_b128 v[230:233], v202 offset:64
	ds_read_b128 v[234:237], v202 offset:96
	ds_read_b128 v[238:241], v202 offset:128
	ds_read_b128 v[242:245], v202 offset:160
	ds_read_b128 v[246:249], v202 offset:192
	ds_read_b128 v[250:253], v202 offset:224
	s_waitcnt lgkmcnt(0)
	s_lshl_b64 s[26:27], s[26:27], 11
	s_add_u32 s7, s61, s26
	s_addc_u32 s26, s62, s27
	s_lshl_b32 s6, s6, 7
	s_and_b32 s6, s6, 0x380
	s_add_u32 s6, s7, s6
	s_mulk_i32 s48, 0x2200
	s_addc_u32 s7, s26, 0
	s_add_i32 s26, s48, 0
	v_mul_lo_u32 v201, v201, s66
	v_lshlrev_b32_e32 v199, 2, v199
	v_mul_f32_e32 v2, v2, v238
	v_mul_f32_e32 v18, v18, v238
	v_add3_u32 v199, s26, v201, v199
	v_fma_f32 v2, v50, v222, -v2
	v_fma_f32 v18, v34, v222, -v18
	ds_write2_b32 v199, v2, v18 offset1:32
	v_mul_f32_e32 v3, v3, v239
	v_mul_f32_e32 v2, v19, v239
	v_fma_f32 v3, v51, v223, -v3
	v_fma_f32 v2, v35, v223, -v2
	ds_write2_b32 v199, v3, v2 offset0:68 offset1:100
	v_mul_f32_e32 v4, v4, v240
	v_mul_f32_e32 v2, v20, v240
	v_fma_f32 v4, v52, v224, -v4
	v_fma_f32 v2, v36, v224, -v2
	ds_write2_b32 v199, v4, v2 offset0:136 offset1:168
	v_mul_f32_e32 v4, v5, v241
	v_mul_f32_e32 v2, v21, v241
	v_fma_f32 v4, v53, v225, -v4
	v_fma_f32 v2, v37, v225, -v2
	ds_write2_b32 v199, v4, v2 offset0:204 offset1:236
	v_mul_f32_e32 v4, v6, v242
	v_mul_f32_e32 v2, v22, v242
	v_fma_f32 v4, v54, v226, -v4
	v_fma_f32 v2, v38, v226, -v2
	v_add_u32_e32 v3, 0x800, v199
	ds_write2_b32 v3, v4, v2 offset0:32 offset1:64
	v_mul_f32_e32 v5, v7, v243
	v_mul_f32_e32 v2, v23, v243
	v_fma_f32 v5, v55, v227, -v5
	v_fma_f32 v2, v39, v227, -v2
	ds_write2_b32 v3, v5, v2 offset0:100 offset1:132
	v_mul_f32_e32 v5, v8, v244
	v_mul_f32_e32 v2, v24, v244
	v_fma_f32 v5, v56, v228, -v5
	v_fma_f32 v2, v40, v228, -v2
	ds_write2_b32 v3, v5, v2 offset0:168 offset1:200
	v_mul_f32_e32 v4, v9, v245
	v_mul_f32_e32 v2, v25, v245
	v_fma_f32 v4, v57, v229, -v4
	v_fma_f32 v2, v41, v229, -v2
	v_add_u32_e32 v3, 0xa00, v199
	ds_write2_b32 v3, v4, v2 offset0:108 offset1:140
	v_mul_f32_e32 v4, v10, v246
	v_mul_f32_e32 v2, v26, v246
	v_fma_f32 v4, v58, v230, -v4
	v_fma_f32 v2, v42, v230, -v2
	v_add_u32_e32 v3, 0x1000, v199
	ds_write2_b32 v3, v4, v2 offset0:64 offset1:96
	v_add_u32_e32 v10, 0x1800, v199
	v_mul_f32_e32 v5, v11, v247
	v_mul_f32_e32 v2, v27, v247
	v_fma_f32 v5, v59, v231, -v5
	v_fma_f32 v2, v43, v231, -v2
	ds_write2_b32 v3, v5, v2 offset0:132 offset1:164
	v_mul_f32_e32 v5, v12, v248
	v_mul_f32_e32 v2, v28, v248
	v_fma_f32 v5, v60, v232, -v5
	v_fma_f32 v2, v44, v232, -v2
	ds_write2_b32 v3, v5, v2 offset0:200 offset1:232
	v_mul_f32_e32 v4, v13, v249
	v_mul_f32_e32 v2, v29, v249
	v_fma_f32 v4, v61, v233, -v4
	v_fma_f32 v2, v45, v233, -v2
	v_add_u32_e32 v3, 0x1400, v199
	ds_write2_b32 v3, v4, v2 offset0:12 offset1:44
	v_mul_f32_e32 v4, v14, v250
	v_mul_f32_e32 v2, v30, v250
	v_fma_f32 v4, v62, v234, -v4
	v_fma_f32 v2, v46, v234, -v2
	ds_write2_b32 v10, v4, v2 offset0:96 offset1:128
	v_lshlrev_b32_e32 v2, 3, v213
	v_and_b32_e32 v30, 56, v2
	v_lshlrev_b32_e32 v11, 2, v30
	global_load_dwordx4 v[6:9], v11, s[8:9]
	global_load_dwordx4 v[2:5], v11, s[8:9] offset:16
	v_mul_f32_e32 v14, v15, v251
	v_mul_f32_e32 v12, v31, v251
	v_fma_f32 v14, v63, v235, -v14
	v_fma_f32 v12, v47, v235, -v12
	ds_write2_b32 v10, v14, v12 offset0:164 offset1:196
	v_xor_b32_e32 v14, 1, v212
	v_cmp_lt_i32_e32 vcc, v14, v196
	v_mul_f32_e32 v13, v16, v252
	v_mul_f32_e32 v10, v32, v252
	v_fma_f32 v13, v64, v236, -v13
	v_fma_f32 v10, v48, v236, -v10
	v_add_u32_e32 v12, 0x1a00, v199
	ds_write2_b32 v12, v13, v10 offset0:104 offset1:136
	v_cndmask_b32_e32 v14, v212, v14, vcc
	v_mul_f32_e32 v13, v17, v253
	v_mul_f32_e32 v10, v33, v253
	v_fma_f32 v13, v65, v237, -v13
	v_fma_f32 v10, v49, v237, -v10
	v_add_u32_e32 v12, 0x1c00, v199
	ds_write2_b32 v12, v13, v10 offset0:44 offset1:76
	v_mul_lo_u32 v10, v200, s66
	v_add3_u32 v32, s26, v10, v11
	ds_read_b128 v[10:13], v32
	v_lshlrev_b32_e32 v33, 2, v14
	ds_read_b128 v[14:17], v32 offset:16
	s_waitcnt lgkmcnt(1)
	v_pk_mul_f32 v[18:19], v[12:13], v[12:13]
	v_pk_mul_f32 v[20:21], v[10:11], v[10:11]
	s_nop 0
	v_pk_mov_b32 v[22:23], v[20:21], v[18:19] op_sel:[1,0]
	v_mov_b32_e32 v21, v19
	v_pk_add_f32 v[18:19], v[22:23], v[20:21]
	s_waitcnt lgkmcnt(0)
	v_pk_mul_f32 v[20:21], v[16:17], v[16:17]
	v_pk_mul_f32 v[22:23], v[14:15], v[14:15]
	v_mov_b32_e32 v24, v20
	v_mov_b32_e32 v25, v22
	v_mov_b32_e32 v22, v21
	v_pk_add_f32 v[20:21], v[24:25], v[22:23]
	v_add_f32_e32 v18, v18, v19
	v_add_f32_e32 v18, v18, v21
	v_add_f32_e32 v18, v20, v18
	v_xor_b32_e32 v20, 2, v212
	v_cmp_lt_i32_e32 vcc, v20, v196
	s_waitcnt lgkmcnt(0)
	s_nop 1
	v_add_f32_dpp v18, v18, v18 quad_perm:[1,0,3,2] row_mask:0xf bank_mask:0xf bound_ctrl:1
	v_cndmask_b32_e32 v20, v212, v20, vcc
	v_lshlrev_b32_e32 v34, 2, v20
	v_xor_b32_e32 v20, 4, v212
	v_cmp_lt_i32_e32 vcc, v20, v196
	v_lshlrev_b32_e32 v196, 1, v30
	s_waitcnt lgkmcnt(0)
	s_nop 1
	v_add_f32_dpp v18, v18, v18 quad_perm:[2,3,0,1] row_mask:0xf bank_mask:0xf bound_ctrl:1
	v_cndmask_b32_e32 v20, v212, v20, vcc
	v_lshlrev_b32_e32 v35, 2, v20
	s_waitcnt lgkmcnt(0)
	s_nop 1
	v_add_f32_dpp v18, v18, v18 row_half_mirror row_mask:0xf bank_mask:0xf bound_ctrl:1
	v_fmamk_f32 v18, v18, 0x3c800000, v211
	v_rsq_f32_e32 v18, v18
	s_nop 0
	v_mul_f32_e32 v18, v195, v18
	v_pk_mul_f32 v[10:11], v[10:11], v[18:19] op_sel_hi:[1,0]
	v_pk_mul_f32 v[12:13], v[12:13], v[18:19] op_sel_hi:[1,0]
	v_pk_mul_f32 v[14:15], v[14:15], v[18:19] op_sel_hi:[1,0]
	v_pk_mul_f32 v[16:17], v[16:17], v[18:19] op_sel_hi:[1,0]
	s_waitcnt vmcnt(1)
; __device__ __forceinline__ u32x4 pack8(const f32x4 a, const f32x4 b) { u32x4 w; w.x = pg8::cvt_pk_bf16(a[0], a[1]); w.y = pg8::cvt_pk_bf16(a[2], a[3]); w.z = pg8::cvt_pk_bf16(b[0], b[1]); w.w = pg8::cvt_pk_bf16(b[2], b[3]); return w; }
; #define LAS __attribute__((address_space(3)))
; template <class Mid> __device__ __forceinline__ void attn_unit(const Mid& mid, LAS unsigned char* lds, const bf16* __restrict__ Qu, const bf16* __restrict__ Kh, const bf16* __restrict__ Vh, int q0, int NT, ...
;     ...
; #pragma unroll
;     for (int ps = 0; ps < 4; ++ps) {
;         const f32x4 x0 = *(const LAS f32x4*)(rb + ps * 8 * OST_PITCH), x1 = *(const LAS f32x4*)(rb + ps * 8 * OST_PITCH + 4);
;         float ss = (x0[0] * x0[0] + x0[1] * x0[1]) + (x0[2] * x0[2] + x0[3] * x0[3]) + (x1[0] * x1[0] + x1[1] * x1[1]) + (x1[2] * x1[2] + x1[3] * x1[3]);
;         ss += __shfl_xor(ss, 1); ss += __shfl_xor(ss, 2); ss += __shfl_xor(ss, 4);
;         const float r = oscale * __builtin_amdgcn_rsqf(ss * (1.0f / 64.0f) + EPS);
;         *(u32x4*)(mrow + (size_t)ps * 8 * DM) = pack8(x0 * r * g0, x1 * r * g1);
;     }
	v_pk_mul_f32 v[12:13], v[8:9], v[12:13]
	v_pk_mul_f32 v[10:11], v[6:7], v[10:11]
	s_waitcnt vmcnt(0)
	v_pk_mul_f32 v[16:17], v[4:5], v[16:17]
	v_pk_mul_f32 v[14:15], v[2:3], v[14:15]
	v_cvt_pk_bf16_f32 v10, v10, v11
	v_cvt_pk_bf16_f32 v11, v12, v13
	s_nop 0
	v_cvt_pk_bf16_f32 v12, v14, v15
	v_cvt_pk_bf16_f32 v13, v16, v17
	ds_read_b128 v[14:17], v32 offset:2176
	ds_read_b128 v[18:21], v32 offset:2192
	s_waitcnt lgkmcnt(1)
	v_pk_mul_f32 v[22:23], v[16:17], v[16:17]
	v_pk_mul_f32 v[24:25], v[14:15], v[14:15]
	s_nop 0
	v_pk_mov_b32 v[26:27], v[24:25], v[22:23] op_sel:[1,0]
	v_mov_b32_e32 v25, v23
	v_pk_add_f32 v[22:23], v[26:27], v[24:25]
	s_waitcnt lgkmcnt(0)
	v_pk_mul_f32 v[24:25], v[20:21], v[20:21]
	v_pk_mul_f32 v[26:27], v[18:19], v[18:19]
	v_mov_b32_e32 v28, v24
	v_mov_b32_e32 v29, v26
	v_mov_b32_e32 v26, v25
	v_pk_add_f32 v[24:25], v[28:29], v[26:27]
	v_add_f32_e32 v22, v22, v23
	v_add_f32_e32 v22, v22, v25
	v_add_f32_e32 v22, v24, v22
	s_waitcnt lgkmcnt(0)
	s_nop 1
	v_add_f32_dpp v22, v22, v22 quad_perm:[1,0,3,2] row_mask:0xf bank_mask:0xf bound_ctrl:1
	s_waitcnt lgkmcnt(0)
	s_nop 1
	v_add_f32_dpp v24, v22, v22 quad_perm:[2,3,0,1] row_mask:0xf bank_mask:0xf bound_ctrl:1
	v_add_u32_e32 v22, s35, v200
	v_ashrrev_i32_e32 v23, 31, v22
	v_lshlrev_b64 v[22:23], 11, v[22:23]
	v_lshl_add_u64 v[22:23], s[6:7], 0, v[22:23]
	s_waitcnt lgkmcnt(0)
	s_nop 1
	v_add_f32_dpp v24, v24, v24 row_half_mirror row_mask:0xf bank_mask:0xf bound_ctrl:1
	v_fmamk_f32 v24, v24, 0x3c800000, v211
	v_rsq_f32_e32 v24, v24
	v_lshl_add_u64 v[22:23], v[22:23], 0, v[196:197]
	global_store_dwordx4 v[22:23], v[10:13], off
	s_mov_b32 s6, 0
	s_nop 0
	v_mul_f32_e32 v10, v195, v24
	v_pk_mul_f32 v[12:13], v[14:15], v[10:11] op_sel_hi:[1,0]
	v_pk_mul_f32 v[14:15], v[16:17], v[10:11] op_sel_hi:[1,0]
	v_pk_mul_f32 v[16:17], v[18:19], v[10:11] op_sel_hi:[1,0]
	v_pk_mul_f32 v[10:11], v[20:21], v[10:11] op_sel_hi:[1,0]
	v_pk_mul_f32 v[14:15], v[8:9], v[14:15]
	v_pk_mul_f32 v[12:13], v[6:7], v[12:13]
	v_pk_mul_f32 v[18:19], v[4:5], v[10:11]
	v_pk_mul_f32 v[16:17], v[2:3], v[16:17]
	v_cvt_pk_bf16_f32 v10, v12, v13
	v_cvt_pk_bf16_f32 v11, v14, v15
	s_nop 0
	v_cvt_pk_bf16_f32 v12, v16, v17
	v_cvt_pk_bf16_f32 v13, v18, v19
	ds_read_b128 v[14:17], v32 offset:4352
	ds_read_b128 v[18:21], v32 offset:4368
	s_waitcnt lgkmcnt(1)
	v_pk_mul_f32 v[24:25], v[16:17], v[16:17]
	v_pk_mul_f32 v[26:27], v[14:15], v[14:15]
	s_nop 0
	v_pk_mov_b32 v[28:29], v[26:27], v[24:25] op_sel:[1,0]
	v_mov_b32_e32 v27, v25
	v_pk_add_f32 v[24:25], v[28:29], v[26:27]
	s_waitcnt lgkmcnt(0)
	v_pk_mul_f32 v[26:27], v[20:21], v[20:21]
	v_pk_mul_f32 v[28:29], v[18:19], v[18:19]
	v_mov_b32_e32 v30, v26
	v_mov_b32_e32 v31, v28
	v_mov_b32_e32 v28, v27
	v_pk_add_f32 v[26:27], v[30:31], v[28:29]
	v_add_f32_e32 v24, v24, v25
	v_add_f32_e32 v24, v24, v27
	v_add_f32_e32 v24, v26, v24
	s_waitcnt lgkmcnt(0)
	s_nop 1
	v_add_f32_dpp v24, v24, v24 quad_perm:[1,0,3,2] row_mask:0xf bank_mask:0xf bound_ctrl:1
	s_waitcnt lgkmcnt(0)
	s_nop 1
	v_add_f32_dpp v24, v24, v24 quad_perm:[2,3,0,1] row_mask:0xf bank_mask:0xf bound_ctrl:1
	s_waitcnt lgkmcnt(0)
	s_nop 1
	v_add_f32_dpp v24, v24, v24 row_half_mirror row_mask:0xf bank_mask:0xf bound_ctrl:1
	v_fmamk_f32 v24, v24, 0x3c800000, v211
	v_rsq_f32_e32 v26, v24
	v_add_co_u32_e32 v24, vcc, s63, v22
	s_nop 1
	v_addc_co_u32_e32 v25, vcc, 0, v23, vcc
	global_store_dwordx4 v[24:25], v[10:13], off
	s_nop 1
	v_mul_f32_e32 v10, v195, v26
	v_pk_mul_f32 v[12:13], v[14:15], v[10:11] op_sel_hi:[1,0]
	v_pk_mul_f32 v[14:15], v[16:17], v[10:11] op_sel_hi:[1,0]
	v_pk_mul_f32 v[16:17], v[18:19], v[10:11] op_sel_hi:[1,0]
	v_pk_mul_f32 v[10:11], v[20:21], v[10:11] op_sel_hi:[1,0]
	v_pk_mul_f32 v[14:15], v[8:9], v[14:15]
	v_pk_mul_f32 v[12:13], v[6:7], v[12:13]
	v_pk_mul_f32 v[18:19], v[4:5], v[10:11]
	v_pk_mul_f32 v[16:17], v[2:3], v[16:17]
	v_cvt_pk_bf16_f32 v10, v12, v13
	v_cvt_pk_bf16_f32 v11, v14, v15
	s_nop 0
	v_cvt_pk_bf16_f32 v12, v16, v17
	v_cvt_pk_bf16_f32 v13, v18, v19
	ds_read_b128 v[14:17], v32 offset:6528
	ds_read_b128 v[18:21], v32 offset:6544
	s_waitcnt lgkmcnt(1)
	v_pk_mul_f32 v[24:25], v[16:17], v[16:17]
	v_pk_mul_f32 v[26:27], v[14:15], v[14:15]
	s_nop 0
	v_pk_mov_b32 v[28:29], v[26:27], v[24:25] op_sel:[1,0]
	v_mov_b32_e32 v27, v25
	v_pk_add_f32 v[24:25], v[28:29], v[26:27]
	s_waitcnt lgkmcnt(0)
	v_pk_mul_f32 v[26:27], v[20:21], v[20:21]
	v_pk_mul_f32 v[28:29], v[18:19], v[18:19]
	v_mov_b32_e32 v30, v26
	v_mov_b32_e32 v31, v28
	v_mov_b32_e32 v28, v27
	v_pk_add_f32 v[26:27], v[30:31], v[28:29]
	v_add_f32_e32 v24, v24, v25
	v_add_f32_e32 v24, v24, v27
	v_add_f32_e32 v24, v26, v24
	s_waitcnt lgkmcnt(0)
	s_nop 1
	v_add_f32_dpp v24, v24, v24 quad_perm:[1,0,3,2] row_mask:0xf bank_mask:0xf bound_ctrl:1
	s_waitcnt lgkmcnt(0)
	s_nop 1
	v_add_f32_dpp v24, v24, v24 quad_perm:[2,3,0,1] row_mask:0xf bank_mask:0xf bound_ctrl:1
	s_waitcnt lgkmcnt(0)
	s_nop 1
	v_add_f32_dpp v24, v24, v24 row_half_mirror row_mask:0xf bank_mask:0xf bound_ctrl:1
	v_fmamk_f32 v24, v24, 0x3c800000, v211
	v_rsq_f32_e32 v26, v24
	v_add_co_u32_e32 v24, vcc, s65, v22
	s_nop 1
	v_addc_co_u32_e32 v25, vcc, 0, v23, vcc
	global_store_dwordx4 v[24:25], v[10:13], off
	s_nop 1
	v_mul_f32_e32 v10, v195, v26
	v_pk_mul_f32 v[12:13], v[14:15], v[10:11] op_sel_hi:[1,0]
	v_pk_mul_f32 v[14:15], v[16:17], v[10:11] op_sel_hi:[1,0]
	v_pk_mul_f32 v[6:7], v[6:7], v[12:13]
	v_pk_mul_f32 v[12:13], v[18:19], v[10:11] op_sel_hi:[1,0]
	v_pk_mul_f32 v[10:11], v[20:21], v[10:11] op_sel_hi:[1,0]
	v_pk_mul_f32 v[8:9], v[8:9], v[14:15]
	v_pk_mul_f32 v[10:11], v[4:5], v[10:11]
	v_pk_mul_f32 v[4:5], v[2:3], v[12:13]
	v_cvt_pk_bf16_f32 v2, v6, v7
	v_add_co_u32_e32 v6, vcc, 0xc000, v22
	v_cvt_pk_bf16_f32 v3, v8, v9
	v_cvt_pk_bf16_f32 v4, v4, v5
	v_cvt_pk_bf16_f32 v5, v10, v11
	s_nop 1
	v_addc_co_u32_e32 v7, vcc, 0, v23, vcc
	s_andn2_b64 vcc, exec, s[28:29]
	global_store_dwordx4 v[6:7], v[2:5], off
	s_cbranch_vccnz .LBB0_446
	s_nop 0
	v_cndmask_b32_e64 v2, 0, 1, s[24:25]
	v_cmp_ne_u32_e64 s[6:7], 1, v2
	v_lshlrev_b32_e32 v2, 1, v198
	s_andn2_b64 vcc, exec, s[24:25]
	v_and_b32_e32 v2, 0x700, v2
	v_mov_b32_e32 v196, v198
	s_cbranch_vccnz .LBB0_470
	s_lshr_b32 s24, s67, 3
	s_and_b32 s24, s24, 0x80
	v_or3_b32 v196, s24, v210, v2

; #define LAS __attribute__((address_space(3)))
; template <class Mid> __device__ __forceinline__ void attn_unit(const Mid& mid, LAS unsigned char* lds, const bf16* __restrict__ Qu, const bf16* __restrict__ Kh, const bf16* __restrict__ Vh, int q0, int NT, ...
;     ...
;     LAS float* wsf = (LAS float*)(lds + FA_WS) + wid * 64;
;     if (hie == 0) { wsf[r32e] = 1.0f / l1; wsf[32 + r32e] = lam / l2; }
;     const LAS float* wq = wsf + 4 * hie;
;     LAS float* sb = (LAS float*)(lds + FA_OST) + wid * (32 * OST_PITCH) + (4 * hie) * OST_PITCH + r32e;
; #pragma unroll
;     for (int i = 0; i < 16; ++i) {
;         const int qc = (i & 3) + 8 * (i >> 2); const float a = wq[qc], b = wq[32 + qc];
;         sb[qc * OST_PITCH] = o1[0][i] * a - o2[0][i] * b; sb[qc * OST_PITCH + 32] = o1[1][i] * a - o2[1][i] * b;
;     }
;     const int ch = lane_e & 7;
;     const f32x4 g0 = *(const f32x4*)(subg + ch * 8), g1 = *(const f32x4*)(subg + ch * 8 + 4);
;     const LAS float* rb = (const LAS float*)(lds + FA_OST) + wid * (32 * OST_PITCH) + (lane_e >> 3) * OST_PITCH + ch * 8;
;     bf16* mrow = mixp + (size_t)(wid * 32 + (lane_e >> 3)) * DM + ch * 8;
; #pragma unroll
;     for (int ps = 0; ps < 4; ++ps) {
;         const f32x4 x0 = *(const LAS f32x4*)(rb + ps * 8 * OST_PITCH), x1 = *(const LAS f32x4*)(rb + ps * 8 * OST_PITCH + 4);
;         float ss = (x0[0] * x0[0] + x0[1] * x0[1]) + (x0[2] * x0[2] + x0[3] * x0[3]) + (x1[0] * x1[0] + x1[1] * x1[1]) + (x1[2] * x1[2] + x1[3] * x1[3]);
;         ss += __shfl_xor(ss, 1); ss += __shfl_xor(ss, 2); ss += __shfl_xor(ss, 4);
.LBB0_1364:
	s_or_b64 exec, exec, s[26:27]
	s_ashr_i32 s26, s65, 3
	s_ashr_i32 s27, s26, 31
	v_ashrrev_i32_e32 v200, 3, v213
	s_lshl_b64 s[26:27], s[26:27], 23
	v_and_b32_e32 v201, -4, v200
	s_add_u32 s5, s57, s26
	s_waitcnt lgkmcnt(0)
	v_lshl_add_u32 v202, v201, 2, s28
	ds_read_b128 v[222:225], v202
	ds_read_b128 v[226:229], v202 offset:32
	ds_read_b128 v[230:233], v202 offset:64
	ds_read_b128 v[234:237], v202 offset:96
	ds_read_b128 v[238:241], v202 offset:128
	ds_read_b128 v[242:245], v202 offset:160
	ds_read_b128 v[246:249], v202 offset:192
	ds_read_b128 v[250:253], v202 offset:224
	s_waitcnt lgkmcnt(0)
	s_addc_u32 s26, s58, s27
	s_lshl_b32 s27, s63, 19
	s_add_u32 s5, s5, s27
	s_addc_u32 s26, s26, 0
	s_lshl_b32 s4, s4, 7
	s_and_b32 s4, s4, 0x380
	s_add_u32 s4, s5, s4
	s_mulk_i32 s66, 0x2200
	s_addc_u32 s5, s26, 0
	s_add_i32 s26, s66, 0
	v_mul_lo_u32 v201, v201, s61
	v_lshlrev_b32_e32 v199, 2, v199
	v_mul_f32_e32 v2, v2, v238
	v_mul_f32_e32 v18, v18, v238
	v_add3_u32 v199, s26, v201, v199
	v_fma_f32 v2, v50, v222, -v2
	v_fma_f32 v18, v34, v222, -v18
	ds_write2_b32 v199, v2, v18 offset1:32
	v_mul_f32_e32 v3, v3, v239
	v_mul_f32_e32 v2, v19, v239
	v_fma_f32 v3, v51, v223, -v3
	v_fma_f32 v2, v35, v223, -v2
	ds_write2_b32 v199, v3, v2 offset0:68 offset1:100
	v_mul_f32_e32 v4, v4, v240
	v_mul_f32_e32 v2, v20, v240
	v_fma_f32 v4, v52, v224, -v4
	v_fma_f32 v2, v36, v224, -v2
	ds_write2_b32 v199, v4, v2 offset0:136 offset1:168
	v_mul_f32_e32 v4, v5, v241
	v_mul_f32_e32 v2, v21, v241
	v_fma_f32 v4, v53, v225, -v4
	v_fma_f32 v2, v37, v225, -v2
	ds_write2_b32 v199, v4, v2 offset0:204 offset1:236
	v_mul_f32_e32 v4, v6, v242
	v_mul_f32_e32 v2, v22, v242
	v_fma_f32 v4, v54, v226, -v4
	v_fma_f32 v2, v38, v226, -v2
	v_add_u32_e32 v3, 0x800, v199
	ds_write2_b32 v3, v4, v2 offset0:32 offset1:64
	v_mul_f32_e32 v5, v7, v243
	v_mul_f32_e32 v2, v23, v243
	v_fma_f32 v5, v55, v227, -v5
	v_fma_f32 v2, v39, v227, -v2
	ds_write2_b32 v3, v5, v2 offset0:100 offset1:132
	v_mul_f32_e32 v5, v8, v244
	v_mul_f32_e32 v2, v24, v244
	v_fma_f32 v5, v56, v228, -v5
	v_fma_f32 v2, v40, v228, -v2
	ds_write2_b32 v3, v5, v2 offset0:168 offset1:200
	v_mul_f32_e32 v4, v9, v245
	v_mul_f32_e32 v2, v25, v245
	v_fma_f32 v4, v57, v229, -v4
	v_fma_f32 v2, v41, v229, -v2
	v_add_u32_e32 v3, 0xa00, v199
	ds_write2_b32 v3, v4, v2 offset0:108 offset1:140
	v_mul_f32_e32 v4, v10, v246
	v_mul_f32_e32 v2, v26, v246
	v_fma_f32 v4, v58, v230, -v4
	v_fma_f32 v2, v42, v230, -v2
	v_add_u32_e32 v3, 0x1000, v199
	ds_write2_b32 v3, v4, v2 offset0:64 offset1:96
	v_add_u32_e32 v10, 0x1800, v199
	v_mul_f32_e32 v5, v11, v247
	v_mul_f32_e32 v2, v27, v247
	v_fma_f32 v5, v59, v231, -v5
	v_fma_f32 v2, v43, v231, -v2
	ds_write2_b32 v3, v5, v2 offset0:132 offset1:164
	v_mul_f32_e32 v5, v12, v248
	v_mul_f32_e32 v2, v28, v248
	v_fma_f32 v5, v60, v232, -v5
	v_fma_f32 v2, v44, v232, -v2
	ds_write2_b32 v3, v5, v2 offset0:200 offset1:232
	v_mul_f32_e32 v4, v13, v249
	v_mul_f32_e32 v2, v29, v249
	v_fma_f32 v4, v61, v233, -v4
	v_fma_f32 v2, v45, v233, -v2
	v_add_u32_e32 v3, 0x1400, v199
	ds_write2_b32 v3, v4, v2 offset0:12 offset1:44
	v_mul_f32_e32 v4, v14, v250
	v_mul_f32_e32 v2, v30, v250
	v_fma_f32 v4, v62, v234, -v4
	v_fma_f32 v2, v46, v234, -v2
	ds_write2_b32 v10, v4, v2 offset0:96 offset1:128
	v_lshlrev_b32_e32 v2, 3, v213
	v_and_b32_e32 v30, 56, v2
	v_lshlrev_b32_e32 v11, 2, v30
	global_load_dwordx4 v[6:9], v11, s[8:9] offset:256
	global_load_dwordx4 v[2:5], v11, s[8:9] offset:272
	v_mul_f32_e32 v14, v15, v251
	v_mul_f32_e32 v12, v31, v251
	v_fma_f32 v14, v63, v235, -v14
	v_fma_f32 v12, v47, v235, -v12
	ds_write2_b32 v10, v14, v12 offset0:164 offset1:196
	v_xor_b32_e32 v14, 1, v212
	v_cmp_lt_i32_e32 vcc, v14, v196
	v_mul_f32_e32 v13, v16, v252
	v_mul_f32_e32 v10, v32, v252
	v_fma_f32 v13, v64, v236, -v13
	v_fma_f32 v10, v48, v236, -v10
	v_add_u32_e32 v12, 0x1a00, v199
	ds_write2_b32 v12, v13, v10 offset0:104 offset1:136
	v_cndmask_b32_e32 v14, v212, v14, vcc
	v_mul_f32_e32 v13, v17, v253
	v_mul_f32_e32 v10, v33, v253
	v_fma_f32 v13, v65, v237, -v13
	v_fma_f32 v10, v49, v237, -v10
	v_add_u32_e32 v12, 0x1c00, v199
	ds_write2_b32 v12, v13, v10 offset0:44 offset1:76
	v_mul_lo_u32 v10, v200, s61
	v_add3_u32 v32, s26, v10, v11
	ds_read_b128 v[10:13], v32
	v_lshlrev_b32_e32 v33, 2, v14
	ds_read_b128 v[14:17], v32 offset:16
	s_waitcnt lgkmcnt(1)
	v_pk_mul_f32 v[18:19], v[12:13], v[12:13]
	v_pk_mul_f32 v[20:21], v[10:11], v[10:11]
	s_nop 0
	v_pk_mov_b32 v[22:23], v[20:21], v[18:19] op_sel:[1,0]
	v_mov_b32_e32 v21, v19
	v_pk_add_f32 v[18:19], v[22:23], v[20:21]
	s_waitcnt lgkmcnt(0)
	v_pk_mul_f32 v[20:21], v[16:17], v[16:17]
	v_pk_mul_f32 v[22:23], v[14:15], v[14:15]
	v_mov_b32_e32 v24, v20
	v_mov_b32_e32 v25, v22
	v_mov_b32_e32 v22, v21
	v_pk_add_f32 v[20:21], v[24:25], v[22:23]
	v_add_f32_e32 v18, v18, v19
	v_add_f32_e32 v18, v18, v21
	v_add_f32_e32 v18, v20, v18
	v_xor_b32_e32 v20, 2, v212
	v_cmp_lt_i32_e32 vcc, v20, v196
	s_waitcnt lgkmcnt(0)
	s_nop 1
	v_add_f32_dpp v18, v18, v18 quad_perm:[1,0,3,2] row_mask:0xf bank_mask:0xf bound_ctrl:1
	v_cndmask_b32_e32 v20, v212, v20, vcc
	v_lshlrev_b32_e32 v34, 2, v20
	v_xor_b32_e32 v20, 4, v212
	v_cmp_lt_i32_e32 vcc, v20, v196
	v_lshlrev_b32_e32 v196, 1, v30
	s_waitcnt lgkmcnt(0)
	s_nop 1
	v_add_f32_dpp v18, v18, v18 quad_perm:[2,3,0,1] row_mask:0xf bank_mask:0xf bound_ctrl:1
	v_cndmask_b32_e32 v20, v212, v20, vcc
	v_lshlrev_b32_e32 v35, 2, v20
	s_waitcnt lgkmcnt(0)
; __device__ __forceinline__ u32x4 pack8(const f32x4 a, const f32x4 b) { u32x4 w; w.x = pg8::cvt_pk_bf16(a[0], a[1]); w.y = pg8::cvt_pk_bf16(a[2], a[3]); w.z = pg8::cvt_pk_bf16(b[0], b[1]); w.w = pg8::cvt_pk_bf16(b[2], b[3]); return w; }
; #define LAS __attribute__((address_space(3)))
; template <class Mid> __device__ __forceinline__ void attn_unit(const Mid& mid, LAS unsigned char* lds, const bf16* __restrict__ Qu, const bf16* __restrict__ Kh, const bf16* __restrict__ Vh, int q0, int NT, ...
;     ...
; #pragma unroll
;     for (int ps = 0; ps < 4; ++ps) {
;         const f32x4 x0 = *(const LAS f32x4*)(rb + ps * 8 * OST_PITCH), x1 = *(const LAS f32x4*)(rb + ps * 8 * OST_PITCH + 4);
;         float ss = (x0[0] * x0[0] + x0[1] * x0[1]) + (x0[2] * x0[2] + x0[3] * x0[3]) + (x1[0] * x1[0] + x1[1] * x1[1]) + (x1[2] * x1[2] + x1[3] * x1[3]);
;         ss += __shfl_xor(ss, 1); ss += __shfl_xor(ss, 2); ss += __shfl_xor(ss, 4);
;         const float r = oscale * __builtin_amdgcn_rsqf(ss * (1.0f / 64.0f) + EPS);
;         *(u32x4*)(mrow + (size_t)ps * 8 * DM) = pack8(x0 * r * g0, x1 * r * g1);
;     }
	s_nop 1
	v_add_f32_dpp v18, v18, v18 row_half_mirror row_mask:0xf bank_mask:0xf bound_ctrl:1
	v_fmamk_f32 v18, v18, 0x3c800000, v211
	v_rsq_f32_e32 v18, v18
	s_nop 0
	v_mul_f32_e32 v18, v195, v18
	v_pk_mul_f32 v[10:11], v[10:11], v[18:19] op_sel_hi:[1,0]
	v_pk_mul_f32 v[12:13], v[12:13], v[18:19] op_sel_hi:[1,0]
	v_pk_mul_f32 v[14:15], v[14:15], v[18:19] op_sel_hi:[1,0]
	v_pk_mul_f32 v[16:17], v[16:17], v[18:19] op_sel_hi:[1,0]
	s_waitcnt vmcnt(1)
	v_pk_mul_f32 v[12:13], v[8:9], v[12:13]
	v_pk_mul_f32 v[10:11], v[6:7], v[10:11]
	s_waitcnt vmcnt(0)
	v_pk_mul_f32 v[16:17], v[4:5], v[16:17]
	v_pk_mul_f32 v[14:15], v[2:3], v[14:15]
	v_cvt_pk_bf16_f32 v10, v10, v11
	v_cvt_pk_bf16_f32 v11, v12, v13
	s_nop 0
	v_cvt_pk_bf16_f32 v12, v14, v15
	v_cvt_pk_bf16_f32 v13, v16, v17
	ds_read_b128 v[14:17], v32 offset:2176
	ds_read_b128 v[18:21], v32 offset:2192
	s_waitcnt lgkmcnt(1)
	v_pk_mul_f32 v[22:23], v[16:17], v[16:17]
	v_pk_mul_f32 v[24:25], v[14:15], v[14:15]
	s_nop 0
	v_pk_mov_b32 v[26:27], v[24:25], v[22:23] op_sel:[1,0]
	v_mov_b32_e32 v25, v23
	v_pk_add_f32 v[22:23], v[26:27], v[24:25]
	s_waitcnt lgkmcnt(0)
	v_pk_mul_f32 v[24:25], v[20:21], v[20:21]
	v_pk_mul_f32 v[26:27], v[18:19], v[18:19]
	v_mov_b32_e32 v28, v24
	v_mov_b32_e32 v29, v26
	v_mov_b32_e32 v26, v25
	v_pk_add_f32 v[24:25], v[28:29], v[26:27]
	v_add_f32_e32 v22, v22, v23
	v_add_f32_e32 v22, v22, v25
	v_add_f32_e32 v22, v24, v22
	s_waitcnt lgkmcnt(0)
	s_nop 1
	v_add_f32_dpp v22, v22, v22 quad_perm:[1,0,3,2] row_mask:0xf bank_mask:0xf bound_ctrl:1
	s_waitcnt lgkmcnt(0)
	s_nop 1
	v_add_f32_dpp v24, v22, v22 quad_perm:[2,3,0,1] row_mask:0xf bank_mask:0xf bound_ctrl:1
	v_add_u32_e32 v22, s29, v200
	v_ashrrev_i32_e32 v23, 31, v22
	v_lshlrev_b64 v[22:23], 11, v[22:23]
	v_lshl_add_u64 v[22:23], s[4:5], 0, v[22:23]
	s_waitcnt lgkmcnt(0)
	s_nop 1
	v_add_f32_dpp v24, v24, v24 row_half_mirror row_mask:0xf bank_mask:0xf bound_ctrl:1
	v_fmamk_f32 v24, v24, 0x3c800000, v211
	v_rsq_f32_e32 v24, v24
	v_lshl_add_u64 v[22:23], v[22:23], 0, v[196:197]
	global_store_dwordx4 v[22:23], v[10:13], off
	s_mov_b32 s4, 0
	s_nop 0
	v_mul_f32_e32 v10, v195, v24
	v_pk_mul_f32 v[12:13], v[14:15], v[10:11] op_sel_hi:[1,0]
	v_pk_mul_f32 v[14:15], v[16:17], v[10:11] op_sel_hi:[1,0]
	v_pk_mul_f32 v[16:17], v[18:19], v[10:11] op_sel_hi:[1,0]
	v_pk_mul_f32 v[10:11], v[20:21], v[10:11] op_sel_hi:[1,0]
	v_pk_mul_f32 v[14:15], v[8:9], v[14:15]
	v_pk_mul_f32 v[12:13], v[6:7], v[12:13]
	v_pk_mul_f32 v[18:19], v[4:5], v[10:11]
	v_pk_mul_f32 v[16:17], v[2:3], v[16:17]
	v_cvt_pk_bf16_f32 v10, v12, v13
	v_cvt_pk_bf16_f32 v11, v14, v15
	s_nop 0
	v_cvt_pk_bf16_f32 v12, v16, v17
	v_cvt_pk_bf16_f32 v13, v18, v19
	ds_read_b128 v[14:17], v32 offset:4352
	ds_read_b128 v[18:21], v32 offset:4368
	s_waitcnt lgkmcnt(1)
	v_pk_mul_f32 v[24:25], v[16:17], v[16:17]
	v_pk_mul_f32 v[26:27], v[14:15], v[14:15]
	s_nop 0
	v_pk_mov_b32 v[28:29], v[26:27], v[24:25] op_sel:[1,0]
	v_mov_b32_e32 v27, v25
	v_pk_add_f32 v[24:25], v[28:29], v[26:27]
	s_waitcnt lgkmcnt(0)
	v_pk_mul_f32 v[26:27], v[20:21], v[20:21]
	v_pk_mul_f32 v[28:29], v[18:19], v[18:19]
	v_mov_b32_e32 v30, v26
	v_mov_b32_e32 v31, v28
	v_mov_b32_e32 v28, v27
	v_pk_add_f32 v[26:27], v[30:31], v[28:29]
	v_add_f32_e32 v24, v24, v25
	v_add_f32_e32 v24, v24, v27
	v_add_f32_e32 v24, v26, v24
	s_waitcnt lgkmcnt(0)
	s_nop 1
	v_add_f32_dpp v24, v24, v24 quad_perm:[1,0,3,2] row_mask:0xf bank_mask:0xf bound_ctrl:1
	s_waitcnt lgkmcnt(0)
	s_nop 1
	v_add_f32_dpp v24, v24, v24 quad_perm:[2,3,0,1] row_mask:0xf bank_mask:0xf bound_ctrl:1
	s_waitcnt lgkmcnt(0)
	s_nop 1
	v_add_f32_dpp v24, v24, v24 row_half_mirror row_mask:0xf bank_mask:0xf bound_ctrl:1
	v_fmamk_f32 v24, v24, 0x3c800000, v211
	v_rsq_f32_e32 v26, v24
	v_add_co_u32_e32 v24, vcc, s59, v22
	s_nop 1
	v_addc_co_u32_e32 v25, vcc, 0, v23, vcc
	global_store_dwordx4 v[24:25], v[10:13], off
	s_nop 1
	v_mul_f32_e32 v10, v195, v26
	v_pk_mul_f32 v[12:13], v[14:15], v[10:11] op_sel_hi:[1,0]
	v_pk_mul_f32 v[14:15], v[16:17], v[10:11] op_sel_hi:[1,0]
	v_pk_mul_f32 v[16:17], v[18:19], v[10:11] op_sel_hi:[1,0]
	v_pk_mul_f32 v[10:11], v[20:21], v[10:11] op_sel_hi:[1,0]
	v_pk_mul_f32 v[14:15], v[8:9], v[14:15]
	v_pk_mul_f32 v[12:13], v[6:7], v[12:13]
	v_pk_mul_f32 v[18:19], v[4:5], v[10:11]
	v_pk_mul_f32 v[16:17], v[2:3], v[16:17]
	v_cvt_pk_bf16_f32 v10, v12, v13
	v_cvt_pk_bf16_f32 v11, v14, v15
	s_nop 0
	v_cvt_pk_bf16_f32 v12, v16, v17
	v_cvt_pk_bf16_f32 v13, v18, v19
	ds_read_b128 v[14:17], v32 offset:6528
	ds_read_b128 v[18:21], v32 offset:6544
	s_waitcnt lgkmcnt(1)
	v_pk_mul_f32 v[24:25], v[16:17], v[16:17]
	v_pk_mul_f32 v[26:27], v[14:15], v[14:15]
	s_nop 0
	v_pk_mov_b32 v[28:29], v[26:27], v[24:25] op_sel:[1,0]
	v_mov_b32_e32 v27, v25
	v_pk_add_f32 v[24:25], v[28:29], v[26:27]
	s_waitcnt lgkmcnt(0)
	v_pk_mul_f32 v[26:27], v[20:21], v[20:21]
	v_pk_mul_f32 v[28:29], v[18:19], v[18:19]
	v_mov_b32_e32 v30, v26
	v_mov_b32_e32 v31, v28
	v_mov_b32_e32 v28, v27
	v_pk_add_f32 v[26:27], v[30:31], v[28:29]
	v_add_f32_e32 v24, v24, v25
	v_add_f32_e32 v24, v24, v27
	v_add_f32_e32 v24, v26, v24
	s_waitcnt lgkmcnt(0)
	s_nop 1
	v_add_f32_dpp v24, v24, v24 quad_perm:[1,0,3,2] row_mask:0xf bank_mask:0xf bound_ctrl:1
	s_waitcnt lgkmcnt(0)
	s_nop 1
	v_add_f32_dpp v24, v24, v24 quad_perm:[2,3,0,1] row_mask:0xf bank_mask:0xf bound_ctrl:1
	s_waitcnt lgkmcnt(0)
	s_nop 1
	v_add_f32_dpp v24, v24, v24 row_half_mirror row_mask:0xf bank_mask:0xf bound_ctrl:1
	v_fmamk_f32 v24, v24, 0x3c800000, v211
	v_rsq_f32_e32 v26, v24
	v_add_co_u32_e32 v24, vcc, s60, v22
	s_nop 1
	v_addc_co_u32_e32 v25, vcc, 0, v23, vcc
	global_store_dwordx4 v[24:25], v[10:13], off
	s_nop 1
	v_mul_f32_e32 v10, v195, v26
	v_pk_mul_f32 v[12:13], v[14:15], v[10:11] op_sel_hi:[1,0]
	v_pk_mul_f32 v[14:15], v[16:17], v[10:11] op_sel_hi:[1,0]
	v_pk_mul_f32 v[6:7], v[6:7], v[12:13]
	v_pk_mul_f32 v[12:13], v[18:19], v[10:11] op_sel_hi:[1,0]
	v_pk_mul_f32 v[10:11], v[20:21], v[10:11] op_sel_hi:[1,0]
	v_pk_mul_f32 v[8:9], v[8:9], v[14:15]
	v_pk_mul_f32 v[10:11], v[4:5], v[10:11]
	v_pk_mul_f32 v[4:5], v[2:3], v[12:13]
	v_cvt_pk_bf16_f32 v2, v6, v7
	v_add_co_u32_e32 v6, vcc, 0xc000, v22
	v_cvt_pk_bf16_f32 v3, v8, v9
	v_cvt_pk_bf16_f32 v4, v4, v5
	v_cvt_pk_bf16_f32 v5, v10, v11
	s_nop 1
	v_addc_co_u32_e32 v7, vcc, 0, v23, vcc
	s_andn2_b64 vcc, exec, s[24:25]
	global_store_dwordx4 v[6:7], v[2:5], off
	s_cbranch_vccnz .LBB0_1351
	s_nop 0
	v_cndmask_b32_e64 v2, 0, 1, s[22:23]
	v_cmp_ne_u32_e64 s[4:5], 1, v2
	v_lshlrev_b32_e32 v2, 1, v198
	s_andn2_b64 vcc, exec, s[22:23]
	v_and_b32_e32 v2, 0x700, v2
	v_mov_b32_e32 v196, v198
	s_cbranch_vccnz .LBB0_1367
	s_lshr_b32 s22, s62, 3
	s_and_b32 s22, s22, 0x80
	v_or3_b32 v196, s22, v210, v2
